# speedup vs baseline: 1.0015x; 1.0015x over previous
.LBB2_12:
	v_cmp_neq_f32_e32 vcc, s25, v102
	v_add_u32_e32 v114, v114, v98
	v_add_u32_e32 v107, 2, v107
	v_cndmask_b32_e64 v124, v112, -v102, vcc
	v_fmamk_f32 v34, v34, 0x3e38aa3b, v124
	v_fmamk_f32 v50, v50, 0x3e38aa3b, v124
	v_exp_f32_e32 v126, v34
	v_fmamk_f32 v34, v51, 0x3e38aa3b, v124
	v_exp_f32_e32 v125, v50
	v_exp_f32_e32 v82, v34
	v_fmamk_f32 v34, v35, 0x3e38aa3b, v124
	v_exp_f32_e32 v34, v34
	v_add_f32_e32 v35, v126, v125
	v_fmamk_f32 v36, v36, 0x3e38aa3b, v124
	v_exp_f32_e32 v127, v36
	v_pk_add_f32 v[50:51], v[34:35], v[82:83]
	v_fmamk_f32 v35, v52, 0x3e38aa3b, v124
	v_pk_add_f32 v[88:89], v[50:51], v[50:51] op_sel_hi:[0,1]
	v_fmamk_f32 v36, v53, 0x3e38aa3b, v124
	v_exp_f32_e32 v35, v35
	s_nop 0
	s_add_i32 s16, s22, 0xffffc000
	s_and_b32 s16, s16, 0xc000
	v_add_u32_e32 v122, s16, v108
	s_add_u32 s16, s12, 0xfffce000
	s_addc_u32 s17, s13, -1
	v_readfirstlane_b32 s26, v122
	v_lshl_add_u64 v[122:123], s[16:17], 0, v[84:85]
	s_mov_b32 s27, m0
	s_mov_b32 m0, s26
	s_nop 0
	global_load_lds_dwordx4 v[122:123], off
	s_mov_b32 m0, s27
	v_lshl_add_u64 v[122:123], s[16:17], 0, v[86:87]
	s_add_i32 s16, s26, 0x400
	s_mov_b32 s17, m0
	s_mov_b32 m0, s16
	s_nop 0
	global_load_lds_dwordx4 v[122:123], off
	s_mov_b32 m0, s17
	s_and_b32 s16, s22, 0xc000
	v_add_u32_e32 v122, s16, v108
	s_nop 0
	v_readfirstlane_b32 s16, v122
	v_lshl_add_u64 v[122:123], s[12:13], 0, v[84:85]
	s_mov_b32 s17, m0
	s_mov_b32 m0, s16
	s_nop 0
	global_load_lds_dwordx4 v[122:123], off
	s_mov_b32 m0, s17
	v_lshl_add_u64 v[122:123], s[12:13], 0, v[86:87]
	s_addk_i32 s16, 0x400
	s_mov_b32 s17, m0
	s_mov_b32 m0, s16
	s_nop 0
	global_load_lds_dwordx4 v[122:123], off
	s_mov_b32 m0, s17
	s_add_u32 s12, s12, 0x64000
	s_addc_u32 s13, s13, 0
	s_add_i32 s22, s22, 0x8000
	v_exp_f32_e32 v88, v36
	v_fmamk_f32 v36, v37, 0x3e38aa3b, v124
	v_exp_f32_e32 v36, v36
	v_add_f32_e32 v37, v127, v35
	v_fmamk_f32 v38, v38, 0x3e38aa3b, v124
	v_exp_f32_e32 v115, v38
	v_pk_add_f32 v[50:51], v[36:37], v[88:89]
	v_fmamk_f32 v37, v54, 0x3e38aa3b, v124
	v_pk_add_f32 v[90:91], v[50:51], v[50:51] op_sel_hi:[0,1]
	v_fmamk_f32 v38, v55, 0x3e38aa3b, v124
	v_exp_f32_e32 v37, v37
	v_exp_f32_e32 v90, v38
	v_fmamk_f32 v38, v39, 0x3e38aa3b, v124
	v_exp_f32_e32 v50, v38
	v_add_f32_e32 v51, v115, v37
	v_pk_add_f32 v[38:39], v[50:51], v[90:91]
	v_pk_add_f32 v[54:55], v[38:39], v[38:39] op_sel_hi:[0,1]
	v_fmamk_f32 v38, v56, 0x3e38aa3b, v124
	v_exp_f32_e32 v51, v38
	v_fmamk_f32 v38, v40, 0x3e38aa3b, v124
	v_exp_f32_e32 v91, v38
	v_fmamk_f32 v38, v57, 0x3e38aa3b, v124
	v_exp_f32_e32 v54, v38
	v_fmamk_f32 v38, v41, 0x3e38aa3b, v124
	v_exp_f32_e32 v52, v38
	v_add_f32_e32 v53, v91, v51
	v_cvt_pk_f16_f32 v57, v51, v54
	v_cvt_pk_f16_f32 v56, v37, v90
	v_pk_add_f32 v[38:39], v[52:53], v[54:55]
	v_cvt_pk_f16_f32 v55, v35, v88
	v_pk_add_f32 v[116:117], v[38:39], v[38:39] op_sel_hi:[0,1]
	v_fmamk_f32 v38, v58, 0x3e38aa3b, v124
	v_exp_f32_e32 v53, v38
	v_fmamk_f32 v38, v42, 0x3e38aa3b, v124
	v_exp_f32_e32 v1, v38
	v_fmamk_f32 v38, v59, 0x3e38aa3b, v124
	v_exp_f32_e32 v116, v38
	v_fmamk_f32 v38, v43, 0x3e38aa3b, v124
	v_exp_f32_e32 v38, v38
	v_add_f32_e32 v39, v1, v53
	v_cvt_pk_f16_f32 v54, v125, v82
	v_fmamk_f32 v35, v64, 0x3e38aa3b, v124
	v_pk_add_f32 v[40:41], v[38:39], v[116:117]
	v_fmamk_f32 v39, v60, 0x3e38aa3b, v124
	v_pk_add_f32 v[118:119], v[40:41], v[40:41] op_sel_hi:[0,1]
	v_fmamk_f32 v40, v44, 0x3e38aa3b, v124
	v_exp_f32_e32 v117, v40
	v_fmamk_f32 v40, v61, 0x3e38aa3b, v124
	v_exp_f32_e32 v39, v39
	v_exp_f32_e32 v118, v40
	v_fmamk_f32 v40, v45, 0x3e38aa3b, v124
	v_exp_f32_e32 v40, v40
	v_add_f32_e32 v41, v117, v39
	v_exp_f32_e32 v82, v35
	v_fmamk_f32 v35, v65, 0x3e38aa3b, v124
	v_pk_add_f32 v[42:43], v[40:41], v[118:119]
	v_fmamk_f32 v41, v62, 0x3e38aa3b, v124
	v_pk_add_f32 v[120:121], v[42:43], v[42:43] op_sel_hi:[0,1]
	v_fmamk_f32 v42, v46, 0x3e38aa3b, v124
	v_exp_f32_e32 v119, v42
	v_fmamk_f32 v42, v63, 0x3e38aa3b, v124
	v_exp_f32_e32 v41, v41
	v_exp_f32_e32 v120, v42
	v_fmamk_f32 v42, v47, 0x3e38aa3b, v124
	v_exp_f32_e32 v122, v42
	ds_read_b64_tr_b16 v[42:43], v114 offset:8192
	ds_read_b64_tr_b16 v[44:45], v114 offset:8704
	v_add_f32_e32 v123, v119, v41
	ds_read_b64_tr_b16 v[58:59], v114 offset:9216
	ds_read_b64_tr_b16 v[60:61], v114 offset:9728
	v_pk_add_f32 v[46:47], v[122:123], v[120:121]
	s_waitcnt lgkmcnt(2)
	v_mfma_f32_32x32x16_f16 v[18:33], v[54:57], v[42:45], v[18:33]
	v_add_f32_e64 v88, v46, v46
	v_add_f32_e64 v89, v46, v47
	ds_read_b64_tr_b16 v[42:43], v114 offset:12288
	ds_read_b64_tr_b16 v[44:45], v114 offset:12800
	v_exp_f32_e32 v88, v35
	ds_read_b64_tr_b16 v[62:63], v114 offset:13312
	ds_read_b64_tr_b16 v[64:65], v114 offset:13824
	v_cvt_pk_f16_f32 v51, v127, v36
	v_cmp_le_u32_e32 vcc, s21, v107
	s_or_b64 s[14:15], vcc, s[14:15]
	s_waitcnt lgkmcnt(2)
	v_mfma_f32_32x32x16_f16 v[2:17], v[54:57], v[42:45], v[2:17]
	v_cvt_pk_f16_f32 v45, v82, v88
	v_cvt_pk_f16_f32 v44, v41, v120
	v_cvt_pk_f16_f32 v43, v39, v118
	v_cvt_pk_f16_f32 v42, v53, v116
	v_cvt_pk_f16_f32 v53, v91, v52
	v_cvt_pk_f16_f32 v52, v115, v50
	v_cvt_pk_f16_f32 v50, v126, v34
	v_mfma_f32_32x32x16_f16 v[18:33], v[42:45], v[58:61], v[18:33]
	v_fmamk_f32 v39, v48, 0x3e38aa3b, v124
	v_fmac_f32_e32 v124, 0x3e38aa3b, v49
	v_exp_f32_e32 v39, v39
	v_exp_f32_e32 v54, v124
	v_cvt_pk_f16_f32 v41, v117, v40
	v_cvt_pk_f16_f32 v40, v1, v38
	v_add_f32_e32 v55, v39, v82
	s_waitcnt lgkmcnt(0)
	v_mfma_f32_32x32x16_f16 v[2:17], v[42:45], v[62:65], v[2:17]
	ds_read_b64_tr_b16 v[42:43], v114 offset:10240
	ds_read_b64_tr_b16 v[44:45], v114 offset:10752
	ds_read_b64_tr_b16 v[34:35], v114 offset:11264
	ds_read_b64_tr_b16 v[36:37], v114 offset:11776
	s_waitcnt lgkmcnt(2)
	v_mfma_f32_32x32x16_f16 v[18:33], v[50:53], v[42:45], v[18:33]
	ds_read_b64_tr_b16 v[42:43], v114 offset:14336
	ds_read_b64_tr_b16 v[44:45], v114 offset:14848
	ds_read_b64_tr_b16 v[46:47], v114 offset:15360
	ds_read_b64_tr_b16 v[48:49], v114 offset:15872
	s_waitcnt lgkmcnt(2)
	v_mfma_f32_32x32x16_f16 v[2:17], v[50:53], v[42:45], v[2:17]
	v_cvt_pk_f16_f32 v43, v39, v54
	v_cvt_pk_f16_f32 v42, v119, v122
	s_nop 1
	v_mfma_f32_32x32x16_f16 v[18:33], v[40:43], v[34:37], v[18:33]
	v_add_f32_e64 v34, v54, v88
	v_add_f32_e64 v35, v55, v89
	v_mov_b32_e32 v88, v102
	v_add_f32_e32 v1, v34, v35
	v_add_f32_e32 v113, v113, v1
	s_waitcnt lgkmcnt(0)
	v_mfma_f32_32x32x16_f16 v[2:17], v[40:43], v[46:49], v[2:17]
	s_andn2_b64 exec, exec, s[14:15]
	s_cbranch_execz .LBB2_17
